# combo7 = combo6 + router-weight conversion loads batched (40 workgroups tail of phase 1)
# speedup vs baseline: 1.0050x; 1.0050x over previous
.LBB0_245:
	s_waitcnt vmcnt(0)
	v_lshl_or_b32 v12, s2, 9, v0
	s_movk_i32 s6, 0x5000
	v_cmp_gt_i32_e32 vcc, s6, v12
	s_and_saveexec_b64 s[6:7], vcc
	s_cbranch_execz .LBB0_296
	s_load_dwordx4 s[8:11], s[0:1], 0x68
	s_load_dwordx2 s[24:25], s[0:1], 0x80
	v_ashrrev_i32_e32 v4, 8, v12
	v_lshlrev_b32_e32 v2, 3, v0
	v_lshl_or_b32 v13, s2, 12, v2
	v_and_b32_e32 v14, 0x7f8, v13
	v_mov_b32_e32 v3, 0
	v_mov_b32_e32 v5, 0
	s_waitcnt lgkmcnt(0)
	s_add_u32 s20, s4, 0x150000
	s_addc_u32 s21, s5, 0
	s_add_u32 s22, s4, 0x1a0000
	s_addc_u32 s23, s5, 0
	v_lshlrev_b32_e32 v6, 2, v14
	s_mov_b64 s[30:31], exec
	s_waitcnt lgkmcnt(0)
	global_load_dwordx4 v[40:43], v6, s[8:9]
	global_load_dwordx4 v[44:47], v6, s[8:9] offset:16
	v_mov_b32_e32 v30, 0
	v_mov_b32_e32 v31, 0
	v_mov_b32_e32 v32, 0
	v_mov_b32_e32 v33, 0
	v_mov_b32_e32 v34, 0
	v_mov_b32_e32 v35, 0
	v_mov_b32_e32 v36, 0
	v_mov_b32_e32 v37, 0
	v_cmp_gt_i32_e32 vcc, 8, v4
	s_and_b64 exec, s[30:31], vcc
	s_cbranch_execz .Lrw_b
	v_lshlrev_b32_e32 v7, 5, v14
	v_lshl_add_u32 v7, v4, 2, v7
	global_load_dword v30, v7, s[10:11]
	global_load_dword v31, v7, s[10:11] offset:32
	global_load_dword v32, v7, s[10:11] offset:64
	global_load_dword v33, v7, s[10:11] offset:96
	global_load_dword v34, v7, s[10:11] offset:128
	global_load_dword v35, v7, s[10:11] offset:160
	global_load_dword v36, v7, s[10:11] offset:192
	global_load_dword v37, v7, s[10:11] offset:224
.Lrw_b:
	s_mov_b64 exec, s[30:31]
	s_movk_i32 s26, 0x48
	v_cmp_lt_i32_e32 vcc, 7, v4
	v_cmp_gt_i32_e64 s[28:29], s26, v4
	s_and_b64 s[28:29], vcc, s[28:29]
	s_and_b64 exec, s[30:31], s[28:29]
	s_cbranch_execz .Lrw_c
	v_lshlrev_b32_e32 v7, 8, v14
	v_lshl_add_u32 v7, v4, 2, v7
	v_subrev_u32_e32 v7, 32, v7
	global_load_dword v30, v7, s[24:25]
	global_load_dword v31, v7, s[24:25] offset:256
	global_load_dword v32, v7, s[24:25] offset:512
	global_load_dword v33, v7, s[24:25] offset:768
	global_load_dword v34, v7, s[24:25] offset:1024
	global_load_dword v35, v7, s[24:25] offset:1280
	global_load_dword v36, v7, s[24:25] offset:1536
	global_load_dword v37, v7, s[24:25] offset:1792
.Lrw_c:
	s_mov_b64 exec, s[30:31]
	s_waitcnt vmcnt(0)
	v_mul_f32_e32 v50, v30, v40
	v_cvt_pk_bf16_f32 v60, v50, v3
	v_mul_f32_e32 v51, v31, v41
	v_cvt_pk_bf16_f32 v61, v51, v3
	v_mul_f32_e32 v52, v32, v42
	v_cvt_pk_bf16_f32 v62, v52, v3
	v_mul_f32_e32 v53, v33, v43
	v_cvt_pk_bf16_f32 v63, v53, v3
	v_mul_f32_e32 v54, v34, v44
	v_cvt_pk_bf16_f32 v64, v54, v3
	v_mul_f32_e32 v55, v35, v45
	v_cvt_pk_bf16_f32 v65, v55, v3
	v_mul_f32_e32 v56, v36, v46
	v_cvt_pk_bf16_f32 v66, v56, v3
	v_mul_f32_e32 v57, v37, v47
	v_cvt_pk_bf16_f32 v67, v57, v3
	v_lshlrev_b32_e32 v60, 16, v60
	v_lshlrev_b32_e32 v61, 16, v61
	v_lshlrev_b32_e32 v62, 16, v62
	v_lshlrev_b32_e32 v63, 16, v63
	v_lshlrev_b32_e32 v64, 16, v64
	v_lshlrev_b32_e32 v65, 16, v65
	v_lshlrev_b32_e32 v66, 16, v66
	v_lshlrev_b32_e32 v67, 16, v67
	v_sub_f32_e32 v70, v50, v60
	v_sub_f32_e32 v71, v51, v61
	v_sub_f32_e32 v72, v52, v62
	v_sub_f32_e32 v73, v53, v63
	v_sub_f32_e32 v74, v54, v64
	v_sub_f32_e32 v75, v55, v65
	v_sub_f32_e32 v76, v56, v66
	v_fma_f32 v77, v37, v47, -v67
	v_cvt_pk_bf16_f32 v80, v60, v61
	v_cvt_pk_bf16_f32 v81, v62, v63
	v_cvt_pk_bf16_f32 v82, v64, v65
	v_cvt_pk_bf16_f32 v83, v66, v67
	v_cvt_pk_bf16_f32 v84, v70, v71
	v_cvt_pk_bf16_f32 v85, v72, v73
	v_cvt_pk_bf16_f32 v86, v74, v75
	v_cvt_pk_bf16_f32 v87, v76, v77
	v_lshlrev_b64 v[4:5], 12, v[4:5]
	v_lshlrev_b32_e32 v2, 1, v14
	v_lshl_add_u64 v[20:21], s[20:21], 0, v[4:5]
	v_lshl_add_u64 v[22:23], s[22:23], 0, v[4:5]
	v_lshl_add_u64 v[20:21], v[20:21], 0, v[2:3]
	v_lshl_add_u64 v[22:23], v[22:23], 0, v[2:3]
	global_store_dwordx4 v[20:21], v[80:83], off
	global_store_dwordx4 v[22:23], v[84:87], off
